# v16_fast
# speedup vs baseline: 1.0362x; 1.0038x over previous
.Lp1_lds_1:
	v_mov_b32_e32 v72, v68
	s_nop 0
	ds_read2_b32 v[66:67], v72 offset1:68
	ds_read2_b32 v[68:69], v72 offset0:136 offset1:204
	s_waitcnt lgkmcnt(0)
	s_branch .Lp1_go_1
.Lp1_fast_1:
	s_add_i32 s84, s84, 1
	v_add_u32_e32 v162, 0x1100, v162
	v_add_u32_e32 v161, 0x1140, v161
	s_cmp_lg_u32 s56, 4
	v_add_u32_e32 v160, 0x1140, v160
	s_cbranch_scc0 .LBB1_125
	s_mov_b32 s59, s56
	s_mov_b64 s[54:55], -1
	s_lshl_b32 s96, s59, 4
	v_or_b32_e32 v164, s96, v131
	v_lshlrev_b32_e32 v163, 2, v164
	v_or_b32_e32 v66, s96, v130
	v_mul_lo_u32 v165, v66, s95
	v_add3_u32 v68, v163, v165, s85
	v_accvgpr_read_b32 v66, a0
	v_accvgpr_read_b32 v67, a1
	v_accvgpr_read_b32 v68, a2
	v_accvgpr_read_b32 v69, a3

.Lp1_lds_2:
	v_mov_b32_e32 v8, v4
	s_nop 0
	ds_read2_b32 v[2:3], v8 offset1:68
	ds_read2_b32 v[4:5], v8 offset0:136 offset1:204
	s_waitcnt lgkmcnt(0)
	s_branch .Lp1_go_2
.Lp1_fast_2:
	s_add_i32 s94, s94, 1
	v_add_u32_e32 v145, 0x1100, v145
	v_add_u32_e32 v147, 0x1140, v147
	s_cmp_lg_u32 s56, 4
	v_add_u32_e32 v11, 0x1140, v11
	s_cbranch_scc0 .LBB1_246
	s_mov_b32 s59, s56
	s_mov_b64 s[52:53], -1
	s_lshl_b32 s97, s59, 4
	v_or_b32_e32 v14, s97, v131
	v_lshlrev_b32_e32 v13, 2, v14
	v_or_b32_e32 v2, s97, v130
	v_mul_lo_u32 v15, v2, s57
	v_add3_u32 v4, v13, v15, s95
	v_accvgpr_read_b32 v2, a0
	v_accvgpr_read_b32 v3, a1
	v_accvgpr_read_b32 v4, a2
	v_accvgpr_read_b32 v5, a3

.Lp1_fast_3:
	s_add_i32 s68, s68, 1
	v_add_u32_e32 v40, 0x1100, v40
	v_add_u32_e32 v39, 0x1140, v39
	s_cmp_lg_u32 s52, 4
	v_add_u32_e32 v38, 0x1140, v38
	s_cbranch_scc0 .LBB1_316
	s_mov_b32 s79, s52
	s_mov_b64 s[52:53], -1
	s_lshl_b32 s80, s79, 4
	v_or_b32_e32 v42, s80, v19
	v_lshlrev_b32_e32 v41, 2, v42
	v_or_b32_e32 v2, s80, v18
	v_mul_lo_u32 v44, v2, s78
	v_add3_u32 v4, v41, v44, s69
	v_accvgpr_read_b32 v2, a0
	v_accvgpr_read_b32 v3, a1
	v_accvgpr_read_b32 v4, a2
	v_accvgpr_read_b32 v5, a3

.Lp1_lds_4:
	v_mov_b32_e32 v6, v2
	s_nop 0
	ds_read2_b32 v[0:1], v6 offset1:68
	ds_read2_b32 v[2:3], v6 offset0:136 offset1:204
	s_waitcnt lgkmcnt(0)
	s_branch .Lp1_go_4
.Lp1_fast_4:
	s_add_i32 s65, s65, 1
	v_add_u32_e32 v30, 0x1100, v30
	v_add_u32_e32 v32, 0x1140, v32
	s_cmp_lg_u32 s52, 4
	v_add_u32_e32 v12, 0x1140, v12
	s_cbranch_scc0 .LBB1_357
	s_mov_b32 s74, s52
	s_mov_b64 s[52:53], -1
	s_lshl_b32 s75, s74, 4
	v_or_b32_e32 v34, s75, v19
	v_lshlrev_b32_e32 v14, 2, v34
	v_or_b32_e32 v0, s75, v18
	v_mul_lo_u32 v35, v0, s64
	v_add3_u32 v2, v14, v35, s72
	v_accvgpr_read_b32 v0, a0
	v_accvgpr_read_b32 v1, a1
	v_accvgpr_read_b32 v2, a2
	v_accvgpr_read_b32 v3, a3
